# half-unit attention: DMA only the used 128-B half of each K row (one K piece per wave per tile, 8 KB K image)
# baseline (speedup 1.0000x reference)
; __device__ __forceinline__ int v_st(int k, int c) { const int kk = (k & ~0xC) | ((k & 4) << 1) | ((k & 8) >> 1); return ((kk >> 3) * 4 + (c >> 5)) * 512 + ((kk & 7) * 32 + (c & 31)) * 2; }
; __device__ __forceinline__ int v_rd_base(int lane) { return ((lane & 3) << 3) | (((lane >> 2) & 3) << 6) | (((lane >> 4) & 1) << 5) | (((lane >> 5) & 1) << 8); }
; #define SWRITE(b, i) do { *(LAS bf16x8*)(V_lds + (b) * SHM_V + vst0) = sr_[i].vs0;          \
;     *(LAS bf16x8*)(V_lds + (b) * SHM_V + vst1) = sr_[i].vs1; int kc = sc * 2;               \
;     *(LAS bf16x8*)(K_lds + (b) * SHM_K + KSWZ(sr, kc)) = sr_[i].ks0;                       \
;     *(LAS bf16x8*)(K_lds + (b) * SHM_K + KSWZ(32 + sr, kc)) = sr_[i].ks1; } while (0)
; #define SWAIT() asm volatile("s_waitcnt vmcnt(4)" ::: "memory")
; template <bool HALF> __device__ __forceinline__ void dense_body(const bf16_t* __restrict__ Qb, const bf16_t* __restrict__ Kh, const bf16_t* __restrict__ Vh, ...
;     ...
;   const int sr = tid >> 4, sc = (tid & 15) * 8, vst0 = v_st(sr, sc), vst1 = v_st(32 + sr, sc);
;   const int vb0 = (int)(uintptr_t)V_lds + v_rd_base(lane);
;   struct { bf16x8 vs0, vs1, ks0, ks1; } sr_[2];
;   const unsigned ko0 = (unsigned)(sr * LDKK + sc) * 2u, ko1 = ko0 + 32u * LDKK * 2u, vo0 = (unsigned)(sr * LDKV + sc) * 2u, vo1 = vo0 + 32u * LDKV * 2u;
;     ...
;   f32x16 pA0, pA1, pB0, pB1; float mnA, mnB, alA, alB; bf16x8 pa0, pa1, pa2, pa3; const int NT = seq / KVBLK;
;   const char* Kl0 = (const char*)K_lds; const char* Kl1 = (const char*)(K_lds + SHM_K);
;   constexpr int SE = 0, SO = 1;
;   SLOAD(SE, 0); asm volatile("s_waitcnt vmcnt(0)" ::: "memory"); SWRITE(0, SE); __syncthreads();
;   qkt<HALF>(pA0, pA1, Kl0, qr, r32, hi, koff); partialSM(pA0, pA1, m_reg, mnA, alA);
;   SLOAD(SO, KVBLK); if (2 < NT) SLOAD(SE, 2 * KVBLK);
;   SWAIT(); SWRITE(1, SO); __syncthreads();
; template <bool HALF> __device__ __forceinline__ void unit(const P& p, int l, int u, LAS char* lds, int tid) {
;     ...
;   const int kvh = hq < 8 ? (hq >> 2) : 2 + ((hq - 8) >> 1);
;   const bf16_t* Qb = WSP(bf16_t, WS_PROJ) + (size_t)qrow * INW + (hq < 8 ? C_AQ + hq * 128 : C_DQ + (hq - 8) * 64);
;   const bf16_t* Kh = WSP(bf16_t, WS_KALL) + kvh * 128;
;   const bf16_t* Vh = WSP(bf16_t, WS_PROJ) + (kvh < 2 ? C_AV + kvh * 128 : C_DV + (kvh - 2) * 128);
.LBB0_453:
	s_ashr_i32 s18, s3, 2
	s_add_i32 s3, s3, -8
	s_lshr_b32 s3, s3, 1
	s_add_i32 s3, s3, 2
	s_and_b64 s[6:7], s[14:15], exec
	s_cselect_b32 s3, s18, s3
	s_lshl_b32 s6, s3, 7
	s_cmp_lt_i32 s3, 2
	s_movk_i32 s3, 0x1100
	s_cselect_b32 s3, s3, 0x1500
	s_ashr_i32 s7, s6, 31
	s_add_i32 s18, s3, s6
	s_lshl_b64 s[14:15], s[6:7], 1
	v_cvt_pk_bf16_f32 v98, v30, v20
	v_cvt_pk_bf16_f32 v99, v31, v21
	v_cvt_pk_bf16_f32 v100, v32, v18
	v_cvt_pk_bf16_f32 v101, v33, v19
	v_cvt_pk_bf16_f32 v106, v34, v16
	v_cvt_pk_bf16_f32 v107, v35, v17
	v_ashrrev_i32_e32 v16, 4, v44
	v_lshlrev_b32_e32 v17, 3, v44
	s_movk_i32 s3, 0x300
	s_add_u32 s20, s44, s14
	v_and_b32_e32 v18, 0x78, v17
	v_mul_lo_u32 v0, v16, s3
	s_addc_u32 s21, s45, s15
	s_ashr_i32 s19, s18, 31
	v_or_b32_e32 v0, v0, v18
	s_movk_i32 s3, 0x1800
	s_lshl_b64 s[18:19], s[18:19], 1
	v_lshlrev_b32_e32 v50, 1, v0
	v_mul_lo_u32 v0, v16, s3
	s_add_u32 s22, s30, s18
	v_or_b32_e32 v0, v0, v18
	s_addc_u32 s23, s31, s19
	v_lshlrev_b32_e32 v54, 1, v0
	v_cvt_pk_bf16_f32 v108, v40, v10
	v_cvt_pk_bf16_f32 v109, v41, v11
	v_cvt_pk_bf16_f32 v110, v4, v8
	v_cvt_pk_bf16_f32 v111, v5, v9
	v_cvt_pk_bf16_f32 v112, v2, v36
	v_cvt_pk_bf16_f32 v113, v1, v37
	v_cvt_pk_bf16_f32 v102, v24, v6
	v_cvt_pk_bf16_f32 v103, v23, v7
	v_cvt_pk_bf16_f32 v104, v14, v26
	v_cvt_pk_bf16_f32 v105, v13, v27
	v_add_u32_e32 v48, 0xc000, v50
	v_add_u32_e32 v52, 0x60000, v54
	v_readlane_b32 s52, v252, 4
	s_nop 3
	v_and_b32_e32 v236, 63, v44
	v_lshrrev_b32_e32 v237, 4, v236
	s_lshl_b32 s53, s52, 2
	v_add_u32_e32 v239, s53, v237
	v_and_b32_e32 v238, 7, v236
	v_and_b32_e32 v240, 7, v239
	v_xor_b32_e32 v240, v238, v240
	v_bfe_u32 v241, v236, 3, 1
	v_lshl_add_u32 v239, v241, 5, v239
	v_mul_u32_u24_e32 v232, 0x600, v239
	v_lshl_add_u32 v232, v240, 4, v232
	s_and_b32 s54, s17, 0x80
	v_add_u32_e32 v232, s54, v232
	s_lshl_b32 s53, s52, 3
	v_bfe_u32 v237, v236, 2, 3
	v_add_u32_e32 v237, s53, v237
	v_and_b32_e32 v238, 4, v237
	v_and_b32_e32 v239, 8, v237
	v_and_b32_e32 v237, 0xfffffff3, v237
	v_lshl_or_b32 v237, v238, 1, v237
	v_lshrrev_b32_e32 v239, 1, v239
	v_or_b32_e32 v237, v237, v239
	v_mul_u32_u24_e32 v234, 0x3000, v237
	v_lshrrev_b32_e32 v238, 5, v236
	v_lshl_add_u32 v234, v238, 6, v234
	v_and_b32_e32 v238, 3, v236
	v_lshl_add_u32 v234, v238, 4, v234
	v_add_u32_e32 v235, 0x80, v234
	s_lshl_b32 s53, s52, 11
	s_lshl_b32 s52, s52, 10
	s_add_i32 s52, s52, 0x8000
	s_add_i32 m0, s52, 0x0
	s_nop 0
	global_load_lds_dwordx4 v232, s[20:21]
	s_add_i32 m0, s53, 0x0
	s_nop 0
	global_load_lds_dwordx4 v234, s[22:23]
	s_add_i32 m0, s53, 0x400
	s_nop 0
	global_load_lds_dwordx4 v235, s[22:23]
	s_add_u32 s48, s20, 0x18000
	s_addc_u32 s49, s21, 0
	s_add_u32 s50, s22, 0xc0000
	s_addc_u32 s51, s23, 0
	s_add_i32 m0, s52, 0x4000
	s_nop 0
	global_load_lds_dwordx4 v232, s[48:49]
	s_add_i32 m0, s53, 0x4000
	s_nop 0
	global_load_lds_dwordx4 v234, s[50:51]
	s_add_i32 m0, s53, 0x4400
	s_nop 0
	global_load_lds_dwordx4 v235, s[50:51]
	s_add_u32 s48, s48, 0x18000
	s_addc_u32 s49, s49, 0
	s_add_u32 s50, s50, 0xc0000
	s_addc_u32 s51, s51, 0
	v_lshlrev_b32_e32 v20, 4, v180
	v_and_b32_e32 v21, 0xfffff0, v16
	v_lshlrev_b32_e32 v22, 1, v16
	v_lshrrev_b32_e32 v23, 1, v16
	v_and_b32_e32 v24, 3, v16
	v_add_u32_e32 v25, 32, v16
	v_and_b32_e32 v73, 0x70, v20
	v_and_or_b32 v20, v22, 8, v21
	v_and_b32_e32 v19, 0x70, v44
	v_bfe_u32 v17, v17, 5, 2
	v_lshlrev_b32_e32 v16, 8, v16
	v_and_or_b32 v21, v23, 4, v24
	v_lshlrev_b32_e32 v18, 1, v18
	v_and_b32_e32 v22, 0xfffff0, v25
	v_lshlrev_b32_e32 v23, 1, v25
	v_lshlrev_b32_e32 v24, 8, v25
	v_lshrrev_b32_e32 v20, 1, v20
	v_and_b32_e32 v25, 48, v18
	v_and_or_b32 v22, v23, 8, v22
	v_bitop3_b32 v16, v18, v16, v19 bitop3:0xde
	v_bitop3_b32 v18, v18, v24, v19 bitop3:0xde
	v_or_b32_e32 v19, v20, v17
	v_lshlrev_b32_e32 v21, 6, v21
	v_lshrrev_b32_e32 v20, 1, v22
	v_add_u32_e32 v188, 0, v16
	v_lshlrev_b32_e32 v16, 9, v19
	s_mov_b32 s3, 0
	v_lshlrev_b32_e32 v72, 8, v180
	v_or_b32_e32 v17, v20, v17
	v_or3_b32 v16, v16, v21, v25
	v_or_b32_e32 v74, s3, v96
	v_lshlrev_b32_e32 v17, 9, v17
	v_add_u32_e32 v190, 0, v16
	v_bitop3_b32 v16, v74, v72, v73 bitop3:0xde
	v_or3_b32 v17, v17, v21, v25
	v_add_u32_e32 v192, 0, v16
	v_add_u32_e32 v189, 0, v18
	v_add_u32_e32 v191, 0, v17
	s_waitcnt vmcnt(0)
	v_and_b32_e32 v76, 63, v44
	s_add_u32 s6, s20, 0x18000
	s_addc_u32 s7, s21, 0
	s_add_u32 s38, s22, 0xc0000
	s_addc_u32 s39, s23, 0
	s_mov_b32 s64, s65
	s_waitcnt lgkmcnt(0)
	s_barrier
; __device__ __forceinline__ void partialSM(f32x16& p0, f32x16& p1, float& m_reg, float& mn, float& alpha) {
;   constexpr float C = SCALE * 1.4426950408889634f;
;   float pmax = p0[0]; for (int r = 1; r < 16; ++r) pmax = fmaxf(pmax, p0[r]); for (int r = 0; r < 16; ++r) pmax = fmaxf(pmax, p1[r]);
;   { auto rr = __builtin_amdgcn_permlane32_swap(__float_as_uint(pmax), __float_as_uint(pmax), false, false);
;     pmax = fmaxf(__uint_as_float(rr[0]), __uint_as_float(rr[1])); }
;   if (__builtin_expect(__all(pmax - m_reg <= THR / SCALE), 1)) { mn = m_reg; alpha = 1.f; }
;   else { mn = fmaxf(m_reg, pmax); alpha = __builtin_amdgcn_exp2f((m_reg - mn) * C); m_reg = mn; }
;   float mnC = -mn * C;
;   for (int r = 0; r < 16; ++r) p0[r] = fmaf(p0[r], C, mnC); for (int r = 0; r < 16; ++r) p1[r] = fmaf(p1[r], C, mnC);
;   for (int r = 0; r < 16; ++r) p0[r] = __builtin_amdgcn_exp2f(p0[r]);
; }
; __device__ __forceinline__ void finishSM(f32x16& p0, f32x16& p1, float alpha, float& l_reg, bf16x8& pa0, bf16x8& pa1, bf16x8& pa2, bf16x8& pa3) {
;   for (int r = 0; r < 16; ++r) p1[r] = __builtin_amdgcn_exp2f(p1[r]);
;   float ps = 0; for (int r = 0; r < 16; ++r) ps += p0[r]; for (int r = 0; r < 16; ++r) ps += p1[r];
;   { auto rr = __builtin_amdgcn_permlane32_swap(__float_as_uint(ps), __float_as_uint(ps), false, false);
;     ps = __uint_as_float(rr[0]) + __uint_as_float(rr[1]); }
;   l_reg = l_reg * alpha + ps;
;     ...
;   PK4(p0, 0, pa0); PK4(p0, 8, pa1); PK4(p1, 0, pa2); PK4(p1, 8, pa3);
;     ...
; }
; template <bool HALF> __device__ __forceinline__ void qkt(f32x16& p0, f32x16& p1, const char* Ks, const bf16x8* qr, int r32, int hi, int koff) {
;   p0 = f32x16{}; p1 = f32x16{};
;   for (int d0 = 0; d0 < (HALF ? 4 : 8); ++d0) { int cb = (d0 * 16 + hi * 8) * 2 + koff;
;     bf16x8 b0 = *reinterpret_cast<const bf16x8*>(Ks + KSWZ(r32, cb));
;     bf16x8 b1 = *reinterpret_cast<const bf16x8*>(Ks + KSWZ(32 + r32, cb));
;     p0 = __builtin_amdgcn_mfma_f32_32x32x16_bf16(b0, qr[d0], p0, 0, 0, 0);
;     p1 = __builtin_amdgcn_mfma_f32_32x32x16_bf16(b1, qr[d0], p1, 0, 0, 0); }
; }
	ds_read_b128 v[0:3], v192 offset:32768
	ds_read_b128 v[4:7], v192 offset:32896
	s_waitcnt lgkmcnt(1)
	v_mfma_f32_32x32x16_bf16 v[16:31], v[0:3], v[98:101], 0
	v_and_b32_e32 v0, 0x3fffffc0, v44
	v_lshl_add_u32 v183, v0, 2, s46
	v_lshlrev_b32_e32 v0, 4, v76
	v_lshlrev_b32_e32 v8, 3, v76
	v_and_b32_e32 v0, 0xc0, v0
	v_and_or_b32 v9, v8, 24, v0
	v_or_b32_e32 v0, 32, v74
	v_bitop3_b32 v0, v0, v72, v73 bitop3:0xde
	v_add_u32_e32 v193, 0, v0
	s_waitcnt lgkmcnt(0)
	v_mfma_f32_32x32x16_bf16 v[32:47], v[4:7], v[98:101], 0
	ds_read_b128 v[0:3], v193 offset:32768
	ds_read_b128 v[4:7], v193 offset:32896
	s_add_u32 s6, s20, 0x30000
	s_addc_u32 s7, s21, 0
	v_and_b32_e32 v8, 0x100, v8
	s_mov_b32 s66, s65
	s_mov_b32 s67, s65
	s_waitcnt lgkmcnt(1)
	v_mfma_f32_32x32x16_bf16 v[16:31], v[0:3], v[106:109], v[16:31]
	v_lshlrev_b32_e32 v0, 1, v76
	v_and_b32_e32 v10, 32, v0
	v_or_b32_e32 v0, 64, v74
	v_bitop3_b32 v0, v0, v72, v73 bitop3:0xde
	v_add_u32_e32 v195, 0, v0
	ds_read_b128 v[0:3], v195 offset:32768
	v_or3_b32 v77, v9, v10, v8
	s_waitcnt lgkmcnt(1)
	v_mfma_f32_32x32x16_bf16 v[32:47], v[4:7], v[106:109], v[32:47]
	ds_read_b128 v[4:7], v195 offset:32896
	s_mov_b32 s68, s65
	s_mov_b32 s69, s65
	s_mov_b32 s70, s65
	s_mov_b32 s71, s65
	s_mov_b32 s72, s65
	s_mov_b32 s73, s65
	s_waitcnt lgkmcnt(1)
	v_mfma_f32_32x32x16_bf16 v[16:31], v[0:3], v[110:113], v[16:31]
	v_or_b32_e32 v0, 0x60, v74
	v_bitop3_b32 v0, v0, v72, v73 bitop3:0xde
	v_add_u32_e32 v194, 0, v0
	ds_read_b128 v[0:3], v194 offset:32768
	ds_read_b128 v[72:75], v194 offset:32896
	s_add_u32 s6, s22, 0x180000
	s_addc_u32 s7, s23, 0
	s_waitcnt lgkmcnt(2)
	v_mfma_f32_32x32x16_bf16 v[32:47], v[4:7], v[110:113], v[32:47]
	s_mov_b32 s74, s65
	s_mov_b32 s75, s65
	s_waitcnt lgkmcnt(1)
	v_mfma_f32_32x32x16_bf16 v[16:31], v[0:3], v[102:105], v[16:31]
	s_mov_b32 s76, s65
	s_mov_b32 s77, s65
	s_mov_b32 s78, s65
	s_mov_b32 s79, s65
	v_mov_b64_e32 v[0:1], s[64:65]
	v_mov_b32_e32 v55, v97
	v_mov_b32_e32 v53, v97
	s_waitcnt lgkmcnt(0)
	v_mfma_f32_32x32x16_bf16 v[32:47], v[72:75], v[102:105], v[32:47]
	s_nop 2
	v_max_f32_e32 v72, v17, v17
	v_max_f32_e32 v73, v16, v16
	v_max_f32_e32 v72, v73, v72
	v_max3_f32 v72, v72, v18, v19
	v_max3_f32 v72, v72, v20, v21
	v_max3_f32 v72, v72, v22, v23
	v_max3_f32 v72, v72, v24, v25
	v_max3_f32 v72, v72, v26, v27
	v_max3_f32 v72, v72, v28, v29
	v_max3_f32 v72, v72, v30, v31
	v_max3_f32 v72, v72, v32, v33
	v_max3_f32 v72, v72, v34, v35
	v_max3_f32 v72, v72, v36, v37
	v_max3_f32 v72, v72, v38, v39
	v_max3_f32 v72, v72, v40, v41
	v_max3_f32 v72, v72, v42, v43
	v_max3_f32 v72, v72, v44, v45
	v_max3_f32 v72, v72, v46, v47
	v_mov_b32_e32 v73, v72
	s_nop 1
	v_permlane32_swap_b32_e32 v72, v73
	v_max_f32_e32 v73, v73, v73
	v_max_f32_e32 v72, v72, v72
	v_max_f32_e32 v72, v72, v73
	v_add_f32_e32 v73, 0x7149f2ca, v72
	v_cmp_ge_f32_e32 vcc, s87, v73
	s_cmp_eq_u64 vcc, exec
	v_max_f32_e32 v56, 0xf149f2ca, v72
	s_cselect_b64 vcc, -1, 0
	v_cndmask_b32_e32 v150, v56, v217, vcc
	v_sub_f32_e32 v57, 0xf149f2ca, v56
	v_mul_f32_e32 v56, 0xbe0293ee, v150
	v_fmamk_f32 v16, v16, 0x3e0293ee, v56
	v_exp_f32_e32 v147, v16
	v_fmamk_f32 v16, v17, 0x3e0293ee, v56
	v_exp_f32_e32 v160, v16
	v_fmamk_f32 v16, v18, 0x3e0293ee, v56
	v_exp_f32_e32 v148, v16
	v_fmamk_f32 v16, v19, 0x3e0293ee, v56
	v_exp_f32_e32 v161, v16
	v_fmamk_f32 v16, v20, 0x3e0293ee, v56
	v_exp_f32_e32 v149, v16
	v_fmamk_f32 v16, v21, 0x3e0293ee, v56
	v_exp_f32_e32 v170, v16
	v_fmamk_f32 v16, v22, 0x3e0293ee, v56
	v_exp_f32_e32 v159, v16
	v_fmamk_f32 v16, v23, 0x3e0293ee, v56
	v_exp_f32_e32 v171, v16
	v_fmamk_f32 v16, v24, 0x3e0293ee, v56
	v_mul_f32_e32 v57, 0x3e0293ee, v57
	v_exp_f32_e32 v151, v16
	v_fmamk_f32 v16, v25, 0x3e0293ee, v56
	v_exp_f32_e32 v57, v57
	v_exp_f32_e32 v155, v16
	v_fmamk_f32 v16, v26, 0x3e0293ee, v56
	v_exp_f32_e32 v152, v16
	v_fmamk_f32 v16, v27, 0x3e0293ee, v56
	v_exp_f32_e32 v156, v16
	v_fmamk_f32 v16, v28, 0x3e0293ee, v56
	v_exp_f32_e32 v153, v16
	v_fmamk_f32 v16, v29, 0x3e0293ee, v56
	v_pk_fma_f32 v[130:131], v[46:47], s[10:11], v[56:57] op_sel_hi:[1,0,0]
	v_pk_fma_f32 v[136:137], v[44:45], s[10:11], v[56:57] op_sel_hi:[1,0,0]
	v_pk_fma_f32 v[140:141], v[42:43], s[10:11], v[56:57] op_sel_hi:[1,0,0]
	v_pk_fma_f32 v[132:133], v[40:41], s[10:11], v[56:57] op_sel_hi:[1,0,0]
	v_pk_fma_f32 v[134:135], v[38:39], s[10:11], v[56:57] op_sel_hi:[1,0,0]
	v_pk_fma_f32 v[138:139], v[36:37], s[10:11], v[56:57] op_sel_hi:[1,0,0]
	v_pk_fma_f32 v[142:143], v[34:35], s[10:11], v[56:57] op_sel_hi:[1,0,0]
	v_pk_fma_f32 v[144:145], v[32:33], s[10:11], v[56:57] op_sel_hi:[1,0,0]
	v_exp_f32_e32 v157, v16
	v_fmamk_f32 v16, v30, 0x3e0293ee, v56
	v_fmac_f32_e32 v56, 0x3e0293ee, v31
	v_exp_f32_e32 v154, v16
	v_exp_f32_e32 v158, v56
	v_mov_b32_e32 v51, v97
	v_mov_b32_e32 v49, v97
	v_mov_b64_e32 v[14:15], s[78:79]
	v_mov_b64_e32 v[2:3], s[66:67]
	v_mov_b64_e32 v[4:5], s[68:69]
	v_mov_b64_e32 v[6:7], s[70:71]
	v_mov_b64_e32 v[8:9], s[72:73]
	v_mov_b64_e32 v[10:11], s[74:75]
	v_mov_b64_e32 v[12:13], s[76:77]
	v_cndmask_b32_e64 v197, v57, 1.0, vcc
	v_lshl_add_u64 v[162:163], s[18:19], 0, v[54:55]
	v_lshl_add_u64 v[164:165], s[18:19], 0, v[52:53]
	v_lshl_add_u64 v[166:167], s[14:15], 0, v[50:51]
	v_lshl_add_u64 v[168:169], s[14:15], 0, v[48:49]
	v_mov_b64_e32 v[62:63], v[14:15]
	v_mov_b64_e32 v[46:47], v[14:15]
	v_mov_b64_e32 v[30:31], v[14:15]
	s_mov_b32 s3, 4
	v_add_u32_e32 v187, 0, v77
	v_cmp_gt_u32_e64 s[40:41], 32, v76
	v_lshl_add_u32 v184, v180, 2, v183
	v_add_u32_e32 v186, s34, v77
	v_mov_b32_e32 v185, 0
	v_mov_b64_e32 v[60:61], v[12:13]
	v_mov_b64_e32 v[58:59], v[10:11]
	v_mov_b64_e32 v[56:57], v[8:9]
	v_mov_b64_e32 v[54:55], v[6:7]
	v_mov_b64_e32 v[52:53], v[4:5]
	v_mov_b64_e32 v[50:51], v[2:3]
	v_mov_b64_e32 v[48:49], v[0:1]
	v_mov_b64_e32 v[44:45], v[12:13]
	v_mov_b64_e32 v[42:43], v[10:11]
	v_mov_b64_e32 v[40:41], v[8:9]
	v_mov_b64_e32 v[38:39], v[6:7]
	v_mov_b64_e32 v[36:37], v[4:5]
	v_mov_b64_e32 v[34:35], v[2:3]
	v_mov_b64_e32 v[32:33], v[0:1]
	v_mov_b64_e32 v[28:29], v[12:13]
	v_mov_b64_e32 v[26:27], v[10:11]
	v_mov_b64_e32 v[24:25], v[8:9]
	v_mov_b64_e32 v[22:23], v[6:7]
	v_mov_b64_e32 v[20:21], v[4:5]
	v_mov_b64_e32 v[18:19], v[2:3]
	v_mov_b64_e32 v[16:17], v[0:1]
	v_readlane_b32 s78, v255, 23
	s_waitcnt lgkmcnt(0)
	s_barrier
	v_readlane_b32 s79, v255, 24
	s_add_i32 m0, s52, 0x0
	s_nop 0
	global_load_lds_dwordx4 v232, s[48:49]
	s_add_u32 s48, s48, 0x18000
	s_addc_u32 s49, s49, 0
	s_mov_b32 s54, 0
; #define SBAR() __builtin_amdgcn_sched_barrier(0)
; __device__ __forceinline__ void finishSM(f32x16& p0, f32x16& p1, float alpha, float& l_reg, bf16x8& pa0, bf16x8& pa1, bf16x8& pa2, bf16x8& pa3) {
;   for (int r = 0; r < 16; ++r) p1[r] = __builtin_amdgcn_exp2f(p1[r]);
;   float ps = 0; for (int r = 0; r < 16; ++r) ps += p0[r]; for (int r = 0; r < 16; ++r) ps += p1[r];
;   { auto rr = __builtin_amdgcn_permlane32_swap(__float_as_uint(ps), __float_as_uint(ps), false, false);
;     ps = __uint_as_float(rr[0]) + __uint_as_float(rr[1]); }
;   l_reg = l_reg * alpha + ps;
;     ...
;   PK4(p0, 0, pa0); PK4(p0, 8, pa1); PK4(p1, 0, pa2); PK4(p1, 8, pa3);
;     ...
; }
; template <bool HALF> __device__ __forceinline__ void qkt(f32x16& p0, f32x16& p1, const char* Ks, const bf16x8* qr, int r32, int hi, int koff) {
;   p0 = f32x16{}; p1 = f32x16{};
;   for (int d0 = 0; d0 < (HALF ? 4 : 8); ++d0) { int cb = (d0 * 16 + hi * 8) * 2 + koff;
;     bf16x8 b0 = *reinterpret_cast<const bf16x8*>(Ks + KSWZ(r32, cb));
;     bf16x8 b1 = *reinterpret_cast<const bf16x8*>(Ks + KSWZ(32 + r32, cb));
;     p0 = __builtin_amdgcn_mfma_f32_32x32x16_bf16(b0, qr[d0], p0, 0, 0, 0);
;     p1 = __builtin_amdgcn_mfma_f32_32x32x16_bf16(b1, qr[d0], p1, 0, 0, 0); }
; }
; __device__ __forceinline__ int v_st(int k, int c) { const int kk = (k & ~0xC) | ((k & 4) << 1) | ((k & 8) >> 1); return ((kk >> 3) * 4 + (c >> 5)) * 512 + ((kk & 7) * 32 + (c & 31)) * 2; }
; __device__ __forceinline__ int v_rd_base(int lane) { return ((lane & 3) << 3) | (((lane >> 2) & 3) << 6) | (((lane >> 4) & 1) << 5) | (((lane >> 5) & 1) << 8); }
; template <int OFF> __device__ __forceinline__ s16x4 tr_read(int vb) {
;   s16x4 r; asm volatile("ds_read_b64_tr_b16 %0, %1 offset:%2" : "=&v"(r) : "v"(vb), "i"(OFF) : "memory"); return r;
; }
; template <int D0> __device__ __forceinline__ void pv_one(f32x16& od, int vb, bf16x8 pa0, bf16x8 pa1, bf16x8 pa2, bf16x8 pa3) {
;   const s16x4 l0 = tr_read<v_rd_off(D0, 0, 0)>(vb), h0 = tr_read<v_rd_off(D0, 0, 1)>(vb), l1 = tr_read<v_rd_off(D0, 1, 0)>(vb), h1 = tr_read<v_rd_off(D0, 1, 1)>(vb);
;   const s16x4 l2 = tr_read<v_rd_off(D0, 2, 0)>(vb), h2 = tr_read<v_rd_off(D0, 2, 1)>(vb), l3 = tr_read<v_rd_off(D0, 3, 0)>(vb), h3 = tr_read<v_rd_off(D0, 3, 1)>(vb);
;   asm volatile("s_waitcnt lgkmcnt(0)" ::: "memory"); SBAR();
;     ...
;   od = __builtin_amdgcn_mfma_f32_32x32x16_bf16(pa0, PK(l0, h0), od, 0, 0, 0);
.LBB0_454:
	ds_read_b128 v[64:67], v192 offset:49152
	ds_read_b128 v[68:71], v192 offset:49280
	v_add_f32_e32 v146, 0, v147
	v_add_f32_e32 v146, v160, v146
	v_add_f32_e32 v146, v148, v146
	s_waitcnt lgkmcnt(1)
	v_mfma_f32_32x32x16_bf16 v[80:95], v[64:67], v[98:101], 0
	v_add_f32_e32 v146, v161, v146
	v_add_f32_e32 v146, v149, v146
	ds_read_b128 v[172:175], v193 offset:49152
	ds_read_b128 v[198:201], v193 offset:49280
	v_add_f32_e32 v146, v170, v146
	v_add_f32_e32 v146, v159, v146
	v_add_f32_e32 v146, v171, v146
	v_add_f32_e32 v146, v151, v146
	s_waitcnt lgkmcnt(2)
	v_mfma_f32_32x32x16_bf16 v[64:79], v[68:71], v[98:101], 0
	v_add_f32_e32 v146, v155, v146
	v_add_f32_e32 v146, v152, v146
	v_add_f32_e32 v146, v156, v146
	v_exp_f32_e32 v144, v144
	v_add_f32_e32 v146, v153, v146
	v_exp_f32_e32 v145, v145
	v_add_f32_e32 v146, v157, v146
	s_waitcnt lgkmcnt(1)
	v_mfma_f32_32x32x16_bf16 v[80:95], v[172:175], v[106:109], v[80:95]
	s_cmp_eq_u32 s54, 0
	s_cbranch_scc1 .Lmv_h
	s_add_i32 m0, s52, 0x0
	s_nop 0
	global_load_lds_dwordx4 v232, s[48:49]
	s_add_u32 s48, s48, 0x18000
	s_addc_u32 s49, s49, 0
	s_add_i32 m0, s53, 0x4000
	s_nop 0
	global_load_lds_dwordx4 v234, s[50:51]
	s_add_i32 m0, s53, 0x4400
	s_nop 0
	global_load_lds_dwordx4 v235, s[50:51]
	s_add_u32 s50, s50, 0xc0000
	s_addc_u32 s51, s51, 0
.Lmv_h:
	v_exp_f32_e32 v142, v142
	v_add_f32_e32 v146, v154, v146
	v_exp_f32_e32 v143, v143
	v_add_f32_e32 v146, v158, v146
	v_exp_f32_e32 v138, v138
	v_add_f32_e32 v146, v144, v146
	v_exp_f32_e32 v139, v139
	s_waitcnt lgkmcnt(0)
	v_mfma_f32_32x32x16_bf16 v[64:79], v[198:201], v[106:109], v[64:79]
	ds_read_b128 v[172:175], v195 offset:49152
	ds_read_b128 v[198:201], v195 offset:49280
	v_add_f32_e32 v146, v145, v146
	v_exp_f32_e32 v134, v134
	v_add_f32_e32 v146, v142, v146
	v_exp_f32_e32 v135, v135
	v_add_f32_e32 v146, v143, v146
	v_exp_f32_e32 v132, v132
	s_waitcnt lgkmcnt(1)
	v_mfma_f32_32x32x16_bf16 v[80:95], v[172:175], v[110:113], v[80:95]
	v_add_f32_e32 v146, v138, v146
	v_exp_f32_e32 v133, v133
	v_add_f32_e32 v146, v139, v146
	v_exp_f32_e32 v140, v140
	v_add_f32_e32 v146, v134, v146
	v_exp_f32_e32 v141, v141
	v_add_f32_e32 v146, v135, v146
	s_waitcnt lgkmcnt(0)
	v_mfma_f32_32x32x16_bf16 v[64:79], v[198:201], v[110:113], v[64:79]
	ds_read_b128 v[172:175], v194 offset:49152
	ds_read_b128 v[198:201], v194 offset:49280
	v_exp_f32_e32 v136, v136
	v_add_f32_e32 v146, v132, v146
	v_exp_f32_e32 v137, v137
	v_add_f32_e32 v146, v133, v146
	v_exp_f32_e32 v130, v130
	v_add_f32_e32 v146, v140, v146
	s_waitcnt lgkmcnt(1)
	v_mfma_f32_32x32x16_bf16 v[80:95], v[172:175], v[102:105], v[80:95]
	v_exp_f32_e32 v131, v131
	v_add_f32_e32 v146, v141, v146
	v_add_f32_e32 v146, v136, v146
	v_add_f32_e32 v146, v137, v146
	v_add_f32_e32 v146, v130, v146
	s_waitcnt lgkmcnt(0)
	v_mfma_f32_32x32x16_bf16 v[64:79], v[198:201], v[102:105], v[64:79]
	v_add_f32_e32 v198, v131, v146
	v_mov_b32_e32 v199, v198
	v_cvt_pk_bf16_f32 v146, v147, v160
	v_cvt_pk_bf16_f32 v147, v148, v161
	v_cvt_pk_bf16_f32 v148, v149, v170
	v_cvt_pk_bf16_f32 v149, v159, v171
	v_cvt_pk_bf16_f32 v200, v151, v155
	v_cvt_pk_bf16_f32 v201, v152, v156
	v_cvt_pk_bf16_f32 v202, v153, v157
	s_nop 1
	v_permlane32_swap_b32_e32 v198, v199
	v_permlane32_swap_b32_e32 v146, v148
	v_cvt_pk_bf16_f32 v203, v154, v158
	v_permlane32_swap_b32_e32 v200, v202
	v_cvt_pk_bf16_f32 v152, v144, v145
	v_cvt_pk_bf16_f32 v153, v142, v143
	v_cvt_pk_bf16_f32 v154, v138, v139
	v_cvt_pk_bf16_f32 v155, v134, v135
	v_cvt_pk_bf16_f32 v156, v132, v133
	v_cvt_pk_bf16_f32 v157, v140, v141
	v_cvt_pk_bf16_f32 v158, v136, v137
	v_cvt_pk_bf16_f32 v159, v130, v131
	v_permlane32_swap_b32_e32 v147, v149
	v_permlane32_swap_b32_e32 v201, v203
	v_permlane32_swap_b32_e32 v152, v154
	v_permlane32_swap_b32_e32 v153, v155
	v_permlane32_swap_b32_e32 v156, v158
	v_permlane32_swap_b32_e32 v157, v159
	ds_read_b64_tr_b16 v[204:205], v187 offset:0
	ds_read_b64_tr_b16 v[206:207], v187 offset:0x800
	ds_read_b64_tr_b16 v[208:209], v187 offset:0x1000
	ds_read_b64_tr_b16 v[210:211], v187 offset:0x1800
	ds_read_b64_tr_b16 v[212:213], v187 offset:0x2000
	ds_read_b64_tr_b16 v[214:215], v187 offset:0x2800
	ds_read_b64_tr_b16 v[222:223], v187 offset:0x3000
	ds_read_b64_tr_b16 v[224:225], v187 offset:0x3800
	s_waitcnt lgkmcnt(0)
	s_nop 0
	v_mfma_f32_32x32x16_bf16 v[0:15], v[146:149], v[204:207], v[0:15]
	ds_read_b64_tr_b16 v[204:205], v187 offset:0x200
	ds_read_b64_tr_b16 v[206:207], v187 offset:0xa00
	v_mfma_f32_32x32x16_bf16 v[0:15], v[200:203], v[208:211], v[0:15]
	ds_read_b64_tr_b16 v[208:209], v187 offset:0x1200
	ds_read_b64_tr_b16 v[210:211], v187 offset:0x1a00
	v_mfma_f32_32x32x16_bf16 v[0:15], v[152:155], v[212:215], v[0:15]
	ds_read_b64_tr_b16 v[212:213], v187 offset:0x2200
	ds_read_b64_tr_b16 v[214:215], v187 offset:0x2a00
	v_mfma_f32_32x32x16_bf16 v[0:15], v[156:159], v[222:225], v[0:15]
	ds_read_b64_tr_b16 v[222:223], v187 offset:0x3200
	ds_read_b64_tr_b16 v[224:225], v187 offset:0x3a00
	s_waitcnt lgkmcnt(0)
	v_mfma_f32_32x32x16_bf16 v[48:63], v[146:149], v[204:207], v[48:63]
	ds_read_b64_tr_b16 v[204:205], v187 offset:0x400
	ds_read_b64_tr_b16 v[206:207], v187 offset:0xc00
	v_mfma_f32_32x32x16_bf16 v[48:63], v[200:203], v[208:211], v[48:63]
	ds_read_b64_tr_b16 v[208:209], v187 offset:0x1400
	ds_read_b64_tr_b16 v[210:211], v187 offset:0x1c00
	v_mfma_f32_32x32x16_bf16 v[48:63], v[152:155], v[212:215], v[48:63]
	ds_read_b64_tr_b16 v[212:213], v187 offset:0x2400
	ds_read_b64_tr_b16 v[214:215], v187 offset:0x2c00
	v_mfma_f32_32x32x16_bf16 v[48:63], v[156:159], v[222:225], v[48:63]
	ds_read_b64_tr_b16 v[222:223], v187 offset:0x3400
	ds_read_b64_tr_b16 v[224:225], v187 offset:0x3c00
	s_waitcnt lgkmcnt(0)
; #define SBAR() __builtin_amdgcn_sched_barrier(0)
; #define SWAIT() asm volatile("s_waitcnt vmcnt(4)" ::: "memory")
; template <int D0> __device__ __forceinline__ void pv_one(f32x16& od, int vb, bf16x8 pa0, bf16x8 pa1, bf16x8 pa2, bf16x8 pa3) {
;   const s16x4 l0 = tr_read<v_rd_off(D0, 0, 0)>(vb), h0 = tr_read<v_rd_off(D0, 0, 1)>(vb), l1 = tr_read<v_rd_off(D0, 1, 0)>(vb), h1 = tr_read<v_rd_off(D0, 1, 1)>(vb);
;   const s16x4 l2 = tr_read<v_rd_off(D0, 2, 0)>(vb), h2 = tr_read<v_rd_off(D0, 2, 1)>(vb), l3 = tr_read<v_rd_off(D0, 3, 0)>(vb), h3 = tr_read<v_rd_off(D0, 3, 1)>(vb);
;   asm volatile("s_waitcnt lgkmcnt(0)" ::: "memory"); SBAR();
;     ...
;   od = __builtin_amdgcn_mfma_f32_32x32x16_bf16(pa0, PK(l0, h0), od, 0, 0, 0);
;   od = __builtin_amdgcn_mfma_f32_32x32x16_bf16(pa1, PK(l1, h1), od, 0, 0, 0);
;   od = __builtin_amdgcn_mfma_f32_32x32x16_bf16(pa2, PK(l2, h2), od, 0, 0, 0);
;   od = __builtin_amdgcn_mfma_f32_32x32x16_bf16(pa3, PK(l3, h3), od, 0, 0, 0);
;     ...
; }
; __device__ __forceinline__ void pv_d0(f32x16* o, int vb, bf16x8 pa0, bf16x8 pa1, bf16x8 pa2, bf16x8 pa3) {
;   pv_one<0>(o[0], vb, pa0, pa1, pa2, pa3); pv_one<1>(o[1], vb, pa0, pa1, pa2, pa3); pv_one<2>(o[2], vb, pa0, pa1, pa2, pa3); pv_one<3>(o[3], vb, pa0, pa1, pa2, pa3);
; template <bool HALF> __device__ __forceinline__ void dense_body(const bf16_t* __restrict__ Qb, const bf16_t* __restrict__ Kh, const bf16_t* __restrict__ Vh, ...
;     ...
;   f32x16 pA0, pA1, pB0, pB1; float mnA, mnB, alA, alB; bf16x8 pa0, pa1, pa2, pa3; const int NT = seq / KVBLK;
;   const char* Kl0 = (const char*)K_lds; const char* Kl1 = (const char*)(K_lds + SHM_K);
;   constexpr int SE = 0, SO = 1;
;   SLOAD(SE, 0); asm volatile("s_waitcnt vmcnt(0)" ::: "memory"); SWRITE(0, SE); __syncthreads();
;   qkt<HALF>(pA0, pA1, Kl0, qr, r32, hi, koff); partialSM(pA0, pA1, m_reg, mnA, alA);
;   SLOAD(SO, KVBLK); if (2 < NT) SLOAD(SE, 2 * KVBLK);
;   SWAIT(); SWRITE(1, SO); __syncthreads();
;   for (int j = 1; j + 1 < NT; j += 2) {
;     SBAR(); qkt<HALF>(pB0, pB1, Kl1, qr, r32, hi, koff);
;     finishSM(pA0, pA1, alA, l_reg, pa0, pa1, pa2, pa3); SBAR();
;     SLOAD(SO, (j + 2) * KVBLK); SBAR();
;     pv_d0(o, vb0, pa0, pa1, pa2, pa3); partialSM(pB0, pB1, m_reg, mnB, alB);
;     __syncthreads(); SWAIT(); SWRITE(0, SE);
;     RESC(alB); __syncthreads();
	v_mfma_f32_32x32x16_bf16 v[32:47], v[146:149], v[204:207], v[32:47]
	ds_read_b64_tr_b16 v[204:205], v187 offset:0x600
	ds_read_b64_tr_b16 v[206:207], v187 offset:0xe00
	v_mfma_f32_32x32x16_bf16 v[32:47], v[200:203], v[208:211], v[32:47]
	ds_read_b64_tr_b16 v[208:209], v187 offset:0x1600
	ds_read_b64_tr_b16 v[210:211], v187 offset:0x1e00
	v_mfma_f32_32x32x16_bf16 v[32:47], v[152:155], v[212:215], v[32:47]
	ds_read_b64_tr_b16 v[212:213], v187 offset:0x2600
	ds_read_b64_tr_b16 v[214:215], v187 offset:0x2e00
	v_mfma_f32_32x32x16_bf16 v[32:47], v[156:159], v[222:225], v[32:47]
	ds_read_b64_tr_b16 v[222:223], v187 offset:0x3600
	ds_read_b64_tr_b16 v[224:225], v187 offset:0x3e00
	s_waitcnt lgkmcnt(0)
	v_mfma_f32_32x32x16_bf16 v[16:31], v[146:149], v[204:207], v[16:31]
	v_max_f32_e32 v146, v81, v81
	v_max_f32_e32 v147, v80, v80
	v_max_f32_e32 v146, v147, v146
	v_max3_f32 v146, v146, v82, v83
	v_max3_f32 v146, v146, v84, v85
	v_max3_f32 v146, v146, v86, v87
	v_max3_f32 v146, v146, v88, v89
	v_max3_f32 v146, v146, v90, v91
	v_max3_f32 v146, v146, v92, v93
	v_mfma_f32_32x32x16_bf16 v[16:31], v[200:203], v[208:211], v[16:31]
	v_max3_f32 v146, v146, v94, v95
	v_max3_f32 v146, v146, v64, v65
	v_max3_f32 v146, v146, v66, v67
	v_max3_f32 v146, v146, v68, v69
	v_max3_f32 v146, v146, v70, v71
	v_max3_f32 v146, v146, v72, v73
	v_max3_f32 v146, v146, v74, v75
	v_max3_f32 v146, v146, v76, v77
	v_mfma_f32_32x32x16_bf16 v[16:31], v[152:155], v[212:215], v[16:31]
	v_max3_f32 v146, v146, v78, v79
	v_mov_b32_e32 v147, v146
	s_nop 1
	v_permlane32_swap_b32_e32 v146, v147
	v_max_f32_e32 v147, v147, v147
	v_max_f32_e32 v146, v146, v146
	v_max_f32_e32 v146, v146, v147
	v_sub_f32_e32 v147, v146, v150
	v_cmp_ge_f32_e32 vcc, s87, v147
	v_max_f32_e32 v147, v150, v150
	v_max_f32_e32 v146, v147, v146
	v_mfma_f32_32x32x16_bf16 v[16:31], v[156:159], v[222:225], v[16:31]
	v_sub_f32_e32 v147, v150, v146
	v_mul_f32_e32 v147, 0x3e0293ee, v147
	v_exp_f32_e32 v147, v147
	s_cmp_eq_u64 vcc, exec
	s_cselect_b64 s[42:43], -1, 0
	s_waitcnt vmcnt(0)
	s_barrier
	v_cndmask_b32_e64 v200, v147, 1.0, s[42:43]
	v_cmp_gt_f32_e32 vcc, 1.0, v200
	s_cbranch_vccz .LBB0_458
	s_and_saveexec_b64 s[6:7], s[40:41]
	ds_write_b32 v184, v200 offset:128
	s_or_b64 exec, exec, s[6:7]
	s_waitcnt lgkmcnt(0)
	v_add_u32_e32 v147, v183, v96
	ds_read_b128 v[152:155], v147 offset:224
	ds_read_b128 v[156:159], v147 offset:192
	ds_read_b128 v[202:205], v147 offset:160
	ds_read_b128 v[206:209], v147 offset:128
	s_waitcnt lgkmcnt(3)
	v_pk_mul_f32 v[12:13], v[12:13], v[152:153]
	s_waitcnt lgkmcnt(2)
	v_pk_mul_f32 v[8:9], v[8:9], v[156:157]
	s_waitcnt lgkmcnt(1)
	v_pk_mul_f32 v[4:5], v[4:5], v[202:203]
	v_pk_mul_f32 v[14:15], v[14:15], v[154:155]
	v_pk_mul_f32 v[10:11], v[10:11], v[158:159]
	v_pk_mul_f32 v[6:7], v[6:7], v[204:205]
	s_waitcnt lgkmcnt(0)
	v_pk_mul_f32 v[2:3], v[2:3], v[208:209]
	v_pk_mul_f32 v[0:1], v[0:1], v[206:207]
	v_pk_mul_f32 v[60:61], v[60:61], v[152:153]
	v_pk_mul_f32 v[56:57], v[56:57], v[156:157]
	v_pk_mul_f32 v[52:53], v[52:53], v[202:203]
	v_pk_mul_f32 v[62:63], v[62:63], v[154:155]
	v_pk_mul_f32 v[58:59], v[58:59], v[158:159]
	v_pk_mul_f32 v[54:55], v[54:55], v[204:205]
	v_pk_mul_f32 v[50:51], v[50:51], v[208:209]
	v_pk_mul_f32 v[48:49], v[48:49], v[206:207]
	v_pk_mul_f32 v[44:45], v[44:45], v[152:153]
	v_pk_mul_f32 v[40:41], v[40:41], v[156:157]
	v_pk_mul_f32 v[36:37], v[36:37], v[202:203]
	v_pk_mul_f32 v[46:47], v[46:47], v[154:155]
	v_pk_mul_f32 v[42:43], v[42:43], v[158:159]
	v_pk_mul_f32 v[38:39], v[38:39], v[204:205]
	v_pk_mul_f32 v[34:35], v[34:35], v[208:209]
	v_pk_mul_f32 v[32:33], v[32:33], v[206:207]
	v_pk_mul_f32 v[28:29], v[28:29], v[152:153]
	v_pk_mul_f32 v[24:25], v[24:25], v[156:157]
	v_pk_mul_f32 v[20:21], v[20:21], v[202:203]
	v_pk_mul_f32 v[30:31], v[30:31], v[154:155]
	v_pk_mul_f32 v[26:27], v[26:27], v[158:159]
	v_pk_mul_f32 v[22:23], v[22:23], v[204:205]
	v_pk_mul_f32 v[18:19], v[18:19], v[208:209]
	v_pk_mul_f32 v[16:17], v[16:17], v[206:207]
; #define SBAR() __builtin_amdgcn_sched_barrier(0)
; __device__ __forceinline__ void partialSM(f32x16& p0, f32x16& p1, float& m_reg, float& mn, float& alpha) {
;     ...
;   float mnC = -mn * C;
;   for (int r = 0; r < 16; ++r) p0[r] = fmaf(p0[r], C, mnC); for (int r = 0; r < 16; ++r) p1[r] = fmaf(p1[r], C, mnC);
;   for (int r = 0; r < 16; ++r) p0[r] = __builtin_amdgcn_exp2f(p0[r]);
; }
; __device__ __forceinline__ void finishSM(f32x16& p0, f32x16& p1, float alpha, float& l_reg, bf16x8& pa0, bf16x8& pa1, bf16x8& pa2, bf16x8& pa3) {
;   for (int r = 0; r < 16; ++r) p1[r] = __builtin_amdgcn_exp2f(p1[r]);
;   float ps = 0; for (int r = 0; r < 16; ++r) ps += p0[r]; for (int r = 0; r < 16; ++r) ps += p1[r];
;   { auto rr = __builtin_amdgcn_permlane32_swap(__float_as_uint(ps), __float_as_uint(ps), false, false);
;     ps = __uint_as_float(rr[0]) + __uint_as_float(rr[1]); }
;   l_reg = l_reg * alpha + ps;
;     ...
;   PK4(p0, 0, pa0); PK4(p0, 8, pa1); PK4(p1, 0, pa2); PK4(p1, 8, pa3);
;     ...
; }
; template <bool HALF> __device__ __forceinline__ void qkt(f32x16& p0, f32x16& p1, const char* Ks, const bf16x8* qr, int r32, int hi, int koff) {
;   p0 = f32x16{}; p1 = f32x16{};
;   for (int d0 = 0; d0 < (HALF ? 4 : 8); ++d0) { int cb = (d0 * 16 + hi * 8) * 2 + koff;
;     bf16x8 b0 = *reinterpret_cast<const bf16x8*>(Ks + KSWZ(r32, cb));
;     bf16x8 b1 = *reinterpret_cast<const bf16x8*>(Ks + KSWZ(32 + r32, cb));
;     p0 = __builtin_amdgcn_mfma_f32_32x32x16_bf16(b0, qr[d0], p0, 0, 0, 0);
;     p1 = __builtin_amdgcn_mfma_f32_32x32x16_bf16(b1, qr[d0], p1, 0, 0, 0); }
; }
; template <bool HALF> __device__ __forceinline__ void dense_body(const bf16_t* __restrict__ Qb, const bf16_t* __restrict__ Kh, const bf16_t* __restrict__ Vh, ...
;     ...
;     SBAR(); qkt<HALF>(pA0, pA1, Kl0, qr, r32, hi, koff);
;     finishSM(pB0, pB1, alB, l_reg, pa0, pa1, pa2, pa3); SBAR();
;     if (j + 3 < NT) SLOAD(SE, (j + 3) * KVBLK); SBAR();
.LBB0_458:
	v_cndmask_b32_e64 v201, v146, v150, s[42:43]
	v_mul_f32_e32 v202, 0xbe0293ee, v201
	v_fmamk_f32 v80, v80, 0x3e0293ee, v202
	v_fmamk_f32 v81, v81, 0x3e0293ee, v202
	v_fmamk_f32 v82, v82, 0x3e0293ee, v202
	v_fmamk_f32 v83, v83, 0x3e0293ee, v202
	v_fmamk_f32 v84, v84, 0x3e0293ee, v202
	v_fmamk_f32 v85, v85, 0x3e0293ee, v202
	v_fmamk_f32 v86, v86, 0x3e0293ee, v202
	v_fmamk_f32 v87, v87, 0x3e0293ee, v202
	v_fmamk_f32 v88, v88, 0x3e0293ee, v202
	v_fmamk_f32 v89, v89, 0x3e0293ee, v202
	v_fmamk_f32 v90, v90, 0x3e0293ee, v202
	v_fmamk_f32 v91, v91, 0x3e0293ee, v202
	v_fmamk_f32 v92, v92, 0x3e0293ee, v202
	v_fmamk_f32 v93, v93, 0x3e0293ee, v202
	v_fmamk_f32 v94, v94, 0x3e0293ee, v202
	v_fmamk_f32 v95, v95, 0x3e0293ee, v202
	v_exp_f32_e32 v146, v80
	v_exp_f32_e32 v161, v81
	v_exp_f32_e32 v147, v82
	v_exp_f32_e32 v160, v83
	v_exp_f32_e32 v148, v84
	v_exp_f32_e32 v159, v85
	v_exp_f32_e32 v149, v86
	v_exp_f32_e32 v158, v87
	v_exp_f32_e32 v150, v88
	v_exp_f32_e32 v157, v89
	v_exp_f32_e32 v151, v90
	v_exp_f32_e32 v156, v91
	v_exp_f32_e32 v152, v92
	v_exp_f32_e32 v155, v93
	v_exp_f32_e32 v153, v94
	v_exp_f32_e32 v154, v95
	v_fmamk_f32 v211, v64, 0x3e0293ee, v202
	v_fmamk_f32 v221, v65, 0x3e0293ee, v202
	v_fmamk_f32 v222, v66, 0x3e0293ee, v202
	v_fmamk_f32 v223, v67, 0x3e0293ee, v202
	v_fmamk_f32 v224, v68, 0x3e0293ee, v202
	v_fmamk_f32 v204, v69, 0x3e0293ee, v202
	v_fmamk_f32 v205, v70, 0x3e0293ee, v202
	v_fmamk_f32 v206, v71, 0x3e0293ee, v202
	v_fmamk_f32 v207, v72, 0x3e0293ee, v202
	v_fmamk_f32 v208, v73, 0x3e0293ee, v202
	v_fmamk_f32 v209, v74, 0x3e0293ee, v202
	v_fmamk_f32 v210, v75, 0x3e0293ee, v202
	v_fmamk_f32 v203, v76, 0x3e0293ee, v202
	v_fmamk_f32 v225, v77, 0x3e0293ee, v202
	v_fmamk_f32 v226, v78, 0x3e0293ee, v202
	v_fmac_f32_e32 v202, 0x3e0293ee, v79
	s_waitcnt lgkmcnt(0)
	ds_read_b128 v[64:67], v192 offset:32768
	ds_read_b128 v[68:71], v192 offset:32896
	ds_read_b128 v[212:215], v193 offset:32768
	ds_read_b128 v[228:231], v193 offset:32896
	v_exp_f32_e32 v211, v211
	v_exp_f32_e32 v204, v204
	s_waitcnt lgkmcnt(3)
	v_mfma_f32_32x32x16_bf16 v[80:95], v[64:67], v[98:101], 0
	v_exp_f32_e32 v205, v205
	v_exp_f32_e32 v206, v206
	v_exp_f32_e32 v207, v207
	v_exp_f32_e32 v208, v208
	v_exp_f32_e32 v209, v209
	v_exp_f32_e32 v210, v210
	s_waitcnt lgkmcnt(2)
	v_mfma_f32_32x32x16_bf16 v[64:79], v[68:71], v[98:101], 0
	s_waitcnt lgkmcnt(1)
	v_mfma_f32_32x32x16_bf16 v[80:95], v[212:215], v[106:109], v[80:95]
	s_add_i32 m0, s52, 0x4000
	s_nop 0
	global_load_lds_dwordx4 v232, s[48:49]
	s_add_u32 s48, s48, 0x18000
	s_addc_u32 s49, s49, 0
	s_waitcnt lgkmcnt(0)
	v_mfma_f32_32x32x16_bf16 v[64:79], v[228:231], v[106:109], v[64:79]
	ds_read_b128 v[212:215], v195 offset:32768
	ds_read_b128 v[228:231], v195 offset:32896
	s_waitcnt lgkmcnt(1)
	v_mfma_f32_32x32x16_bf16 v[80:95], v[212:215], v[110:113], v[80:95]
	s_waitcnt lgkmcnt(0)
	v_mfma_f32_32x32x16_bf16 v[64:79], v[228:231], v[110:113], v[64:79]
	s_add_i32 m0, s53, 0x0
	s_nop 0
	global_load_lds_dwordx4 v234, s[50:51]
	s_add_i32 m0, s53, 0x400
	s_nop 0
	global_load_lds_dwordx4 v235, s[50:51]
	s_add_u32 s50, s50, 0xc0000
	s_addc_u32 s51, s51, 0
	ds_read_b128 v[212:215], v194 offset:32768
	ds_read_b128 v[228:231], v194 offset:32896
	s_waitcnt lgkmcnt(1)
	v_mfma_f32_32x32x16_bf16 v[80:95], v[212:215], v[102:105], v[80:95]
	v_exp_f32_e32 v215, v224
	v_exp_f32_e32 v224, v202
	v_add_f32_e32 v202, 0, v146
	v_add_f32_e32 v202, v161, v202
	v_add_f32_e32 v202, v147, v202
	v_add_f32_e32 v202, v160, v202
	v_add_f32_e32 v202, v148, v202
	v_add_f32_e32 v202, v159, v202
	v_add_f32_e32 v202, v149, v202
	v_add_f32_e32 v202, v158, v202
	v_add_f32_e32 v202, v150, v202
	v_add_f32_e32 v202, v157, v202
	v_add_f32_e32 v202, v151, v202
	v_add_f32_e32 v202, v156, v202
	v_add_f32_e32 v202, v152, v202
	v_exp_f32_e32 v212, v221
	v_add_f32_e32 v202, v155, v202
	v_exp_f32_e32 v213, v222
	v_add_f32_e32 v202, v153, v202
	v_exp_f32_e32 v214, v223
	v_add_f32_e32 v202, v154, v202
	v_add_f32_e32 v202, v211, v202
	v_add_f32_e32 v202, v212, v202
	v_add_f32_e32 v202, v213, v202
	v_add_f32_e32 v202, v214, v202
	v_add_f32_e32 v202, v215, v202
	v_add_f32_e32 v202, v204, v202
	v_add_f32_e32 v202, v205, v202
	v_add_f32_e32 v202, v206, v202
	v_exp_f32_e32 v221, v203
	v_add_f32_e32 v202, v207, v202
	v_exp_f32_e32 v222, v225
	v_add_f32_e32 v202, v208, v202
	s_waitcnt lgkmcnt(0)
	v_mfma_f32_32x32x16_bf16 v[64:79], v[228:231], v[102:105], v[64:79]
	v_exp_f32_e32 v223, v226
	v_add_f32_e32 v202, v209, v202
	v_add_f32_e32 v202, v210, v202
	v_add_f32_e32 v202, v221, v202
	v_add_f32_e32 v202, v222, v202
	v_add_f32_e32 v202, v223, v202
	v_add_f32_e32 v202, v224, v202
	v_mov_b32_e32 v203, v202
	v_cvt_pk_bf16_f32 v146, v146, v161
	v_cvt_pk_bf16_f32 v147, v147, v160
	v_cvt_pk_bf16_f32 v148, v148, v159
	v_cvt_pk_bf16_f32 v149, v149, v158
	v_cvt_pk_bf16_f32 v150, v150, v157
	v_cvt_pk_bf16_f32 v151, v151, v156
	v_cvt_pk_bf16_f32 v152, v152, v155
	v_cvt_pk_bf16_f32 v153, v153, v154
	v_cvt_pk_bf16_f32 v154, v211, v212
	v_cvt_pk_bf16_f32 v155, v213, v214
	v_cvt_pk_bf16_f32 v156, v215, v204
	v_cvt_pk_bf16_f32 v157, v205, v206
	v_cvt_pk_bf16_f32 v158, v207, v208
	v_cvt_pk_bf16_f32 v159, v209, v210
	v_cvt_pk_bf16_f32 v160, v221, v222
	v_cvt_pk_bf16_f32 v161, v223, v224
	s_nop 1
	v_permlane32_swap_b32_e32 v202, v203
	v_permlane32_swap_b32_e32 v146, v148
	v_permlane32_swap_b32_e32 v147, v149
	v_permlane32_swap_b32_e32 v150, v152
	v_permlane32_swap_b32_e32 v151, v153
	v_permlane32_swap_b32_e32 v154, v156
	v_permlane32_swap_b32_e32 v155, v157
	v_permlane32_swap_b32_e32 v158, v160
	v_permlane32_swap_b32_e32 v159, v161
	s_cmp_ge_u32 s3, s24
	s_cselect_b64 s[14:15], -1, 0

; #define SBAR() __builtin_amdgcn_sched_barrier(0)
; __device__ __forceinline__ void finishSM(f32x16& p0, f32x16& p1, float alpha, float& l_reg, bf16x8& pa0, bf16x8& pa1, bf16x8& pa2, bf16x8& pa3) {
;   for (int r = 0; r < 16; ++r) p1[r] = __builtin_amdgcn_exp2f(p1[r]);
;   float ps = 0; for (int r = 0; r < 16; ++r) ps += p0[r]; for (int r = 0; r < 16; ++r) ps += p1[r];
;   { auto rr = __builtin_amdgcn_permlane32_swap(__float_as_uint(ps), __float_as_uint(ps), false, false);
;     ps = __uint_as_float(rr[0]) + __uint_as_float(rr[1]); }
;   l_reg = l_reg * alpha + ps;
;     ...
;   PK4(p0, 0, pa0); PK4(p0, 8, pa1); PK4(p1, 0, pa2); PK4(p1, 8, pa3);
;     ...
; }
; template <bool HALF> __device__ __forceinline__ void qkt(f32x16& p0, f32x16& p1, const char* Ks, const bf16x8* qr, int r32, int hi, int koff) {
;   p0 = f32x16{}; p1 = f32x16{};
;   for (int d0 = 0; d0 < (HALF ? 4 : 8); ++d0) { int cb = (d0 * 16 + hi * 8) * 2 + koff;
;     bf16x8 b0 = *reinterpret_cast<const bf16x8*>(Ks + KSWZ(r32, cb));
;     bf16x8 b1 = *reinterpret_cast<const bf16x8*>(Ks + KSWZ(32 + r32, cb));
;     p0 = __builtin_amdgcn_mfma_f32_32x32x16_bf16(b0, qr[d0], p0, 0, 0, 0);
;     p1 = __builtin_amdgcn_mfma_f32_32x32x16_bf16(b1, qr[d0], p1, 0, 0, 0); }
; }
; template <bool HALF> __device__ __forceinline__ void dense_body(const bf16_t* __restrict__ Qb, const bf16_t* __restrict__ Kh, const bf16_t* __restrict__ Vh, ...
;     ...
;   SBAR(); qkt<HALF>(pB0, pB1, Kl1, qr, r32, hi, koff);
;   finishSM(pA0, pA1, alA, l_reg, pa0, pa1, pa2, pa3); SBAR();
;   pv_d0(o, vb0, pa0, pa1, pa2, pa3); partialSM(pB0, pB1, m_reg, mnB, alB);
.LBB0_466:
	ds_read_b128 v[64:67], v192 offset:49152
	ds_read_b128 v[68:71], v192 offset:49280
	v_exp_f32_e32 v118, v140
	v_exp_f32_e32 v119, v141
	v_exp_f32_e32 v120, v136
	s_waitcnt lgkmcnt(1)
	v_mfma_f32_32x32x16_bf16 v[80:95], v[64:67], v[98:101], 0
	v_exp_f32_e32 v121, v137
	v_exp_f32_e32 v122, v130
	v_exp_f32_e32 v123, v131
	s_waitcnt lgkmcnt(0)
	v_mfma_f32_32x32x16_bf16 v[64:79], v[68:71], v[98:101], 0
	ds_read_b128 v[98:101], v193 offset:49152
	ds_read_b128 v[114:117], v193 offset:49280
	s_waitcnt lgkmcnt(1)
	v_mfma_f32_32x32x16_bf16 v[80:95], v[98:101], v[106:109], v[80:95]
	s_add_i32 m0, s53, 0x4000
	s_nop 0
	global_load_lds_dwordx4 v234, s[50:51]
	s_add_i32 m0, s53, 0x4400
	s_nop 0
	global_load_lds_dwordx4 v235, s[50:51]
	s_waitcnt lgkmcnt(0)
	v_mfma_f32_32x32x16_bf16 v[64:79], v[114:117], v[106:109], v[64:79]
	ds_read_b128 v[98:101], v195 offset:49152
	ds_read_b128 v[106:109], v195 offset:49280
	v_exp_f32_e32 v114, v134
	v_exp_f32_e32 v115, v135
	v_exp_f32_e32 v116, v132
	v_exp_f32_e32 v117, v133
	s_waitcnt lgkmcnt(1)
	v_mfma_f32_32x32x16_bf16 v[80:95], v[98:101], v[110:113], v[80:95]
	s_waitcnt lgkmcnt(0)
	v_mfma_f32_32x32x16_bf16 v[64:79], v[106:109], v[110:113], v[64:79]
	ds_read_b128 v[98:101], v194 offset:49152
	ds_read_b128 v[106:109], v194 offset:49280
	v_exp_f32_e32 v110, v142
	v_exp_f32_e32 v111, v143
	v_exp_f32_e32 v112, v138
	v_exp_f32_e32 v113, v139
	s_waitcnt lgkmcnt(1)
	v_mfma_f32_32x32x16_bf16 v[80:95], v[98:101], v[102:105], v[80:95]
	v_add_f32_e32 v98, 0, v147
	v_add_f32_e32 v98, v160, v98
	v_add_f32_e32 v98, v148, v98
	v_add_f32_e32 v98, v161, v98
	v_add_f32_e32 v98, v149, v98
	v_add_f32_e32 v98, v170, v98
	v_add_f32_e32 v98, v159, v98
	v_add_f32_e32 v98, v171, v98
	v_add_f32_e32 v98, v151, v98
	v_add_f32_e32 v98, v155, v98
	v_add_f32_e32 v98, v152, v98
	v_add_f32_e32 v98, v156, v98
	s_waitcnt lgkmcnt(0)
	v_mfma_f32_32x32x16_bf16 v[64:79], v[106:109], v[102:105], v[64:79]
	v_exp_f32_e32 v108, v144
	v_add_f32_e32 v98, v153, v98
	v_exp_f32_e32 v109, v145
	v_add_f32_e32 v98, v157, v98
	v_add_f32_e32 v98, v154, v98
	v_add_f32_e32 v98, v158, v98
	v_add_f32_e32 v98, v108, v98
	v_add_f32_e32 v98, v109, v98
	v_add_f32_e32 v98, v110, v98
	v_add_f32_e32 v98, v111, v98
	v_add_f32_e32 v98, v112, v98
	v_add_f32_e32 v98, v113, v98
	v_add_f32_e32 v98, v114, v98
	v_add_f32_e32 v98, v115, v98
	v_add_f32_e32 v98, v116, v98
	v_add_f32_e32 v98, v117, v98
	v_add_f32_e32 v98, v118, v98
	v_add_f32_e32 v98, v119, v98
	v_add_f32_e32 v98, v120, v98
	v_add_f32_e32 v98, v121, v98
	v_add_f32_e32 v98, v122, v98
	v_add_f32_e32 v98, v123, v98
	v_mov_b32_e32 v99, v98
	v_cvt_pk_bf16_f32 v100, v147, v160
	v_cvt_pk_bf16_f32 v101, v148, v161
	v_cvt_pk_bf16_f32 v102, v149, v170
	v_cvt_pk_bf16_f32 v103, v159, v171
	s_nop 1
	v_permlane32_swap_b32_e32 v98, v99
	v_permlane32_swap_b32_e32 v100, v102
	v_permlane32_swap_b32_e32 v101, v103
	v_cvt_pk_bf16_f32 v104, v151, v155
	v_cvt_pk_bf16_f32 v105, v152, v156
	v_cvt_pk_bf16_f32 v106, v153, v157
	v_cvt_pk_bf16_f32 v107, v154, v158
	v_cvt_pk_bf16_f32 v108, v108, v109
	v_cvt_pk_bf16_f32 v109, v110, v111
	v_cvt_pk_bf16_f32 v110, v112, v113
	v_cvt_pk_bf16_f32 v111, v114, v115
	v_cvt_pk_bf16_f32 v112, v116, v117
	v_cvt_pk_bf16_f32 v113, v118, v119
	v_cvt_pk_bf16_f32 v114, v120, v121
	v_cvt_pk_bf16_f32 v115, v122, v123
	s_nop 0
	v_permlane32_swap_b32_e32 v104, v106
	v_permlane32_swap_b32_e32 v105, v107
	v_permlane32_swap_b32_e32 v108, v110
	v_permlane32_swap_b32_e32 v109, v111
	v_permlane32_swap_b32_e32 v112, v114
	v_permlane32_swap_b32_e32 v113, v115
	ds_read_b64_tr_b16 v[116:117], v187 offset:0
	ds_read_b64_tr_b16 v[118:119], v187 offset:0x800
	ds_read_b64_tr_b16 v[120:121], v187 offset:0x1000
	ds_read_b64_tr_b16 v[122:123], v187 offset:0x1800
	ds_read_b64_tr_b16 v[124:125], v187 offset:0x2000
	ds_read_b64_tr_b16 v[126:127], v187 offset:0x2800
	ds_read_b64_tr_b16 v[128:129], v187 offset:0x3000
	ds_read_b64_tr_b16 v[130:131], v187 offset:0x3800
	s_waitcnt lgkmcnt(0)
	s_nop 0
	v_mfma_f32_32x32x16_bf16 v[0:15], v[100:103], v[116:119], v[0:15]
	ds_read_b64_tr_b16 v[116:117], v187 offset:0x200
	ds_read_b64_tr_b16 v[118:119], v187 offset:0xa00
	v_mfma_f32_32x32x16_bf16 v[0:15], v[104:107], v[120:123], v[0:15]
	ds_read_b64_tr_b16 v[120:121], v187 offset:0x1200
	ds_read_b64_tr_b16 v[122:123], v187 offset:0x1a00
	v_mfma_f32_32x32x16_bf16 v[0:15], v[108:111], v[124:127], v[0:15]
	ds_read_b64_tr_b16 v[124:125], v187 offset:0x2200
	ds_read_b64_tr_b16 v[126:127], v187 offset:0x2a00
	v_mfma_f32_32x32x16_bf16 v[0:15], v[112:115], v[128:131], v[0:15]
	ds_read_b64_tr_b16 v[128:129], v187 offset:0x3200
	ds_read_b64_tr_b16 v[130:131], v187 offset:0x3a00
	s_waitcnt lgkmcnt(0)
; #define SBAR() __builtin_amdgcn_sched_barrier(0)
; #define RESC(a) do { if (__any((a) < 1.f)) { if (hi == 0) al_l[r32] = (a); asm volatile("s_waitcnt lgkmcnt(0)" ::: "memory"); \
;     for (int d = 0; d < 4; ++d) for (int r = 0; r < 16; ++r) o[d][r] *= al_l[crow(r, hi)]; } } while (0)
; template <int D0> __device__ __forceinline__ void pv_one(f32x16& od, int vb, bf16x8 pa0, bf16x8 pa1, bf16x8 pa2, bf16x8 pa3) {
;   const s16x4 l0 = tr_read<v_rd_off(D0, 0, 0)>(vb), h0 = tr_read<v_rd_off(D0, 0, 1)>(vb), l1 = tr_read<v_rd_off(D0, 1, 0)>(vb), h1 = tr_read<v_rd_off(D0, 1, 1)>(vb);
;   const s16x4 l2 = tr_read<v_rd_off(D0, 2, 0)>(vb), h2 = tr_read<v_rd_off(D0, 2, 1)>(vb), l3 = tr_read<v_rd_off(D0, 3, 0)>(vb), h3 = tr_read<v_rd_off(D0, 3, 1)>(vb);
;   asm volatile("s_waitcnt lgkmcnt(0)" ::: "memory"); SBAR();
;     ...
;   od = __builtin_amdgcn_mfma_f32_32x32x16_bf16(pa0, PK(l0, h0), od, 0, 0, 0);
;   od = __builtin_amdgcn_mfma_f32_32x32x16_bf16(pa1, PK(l1, h1), od, 0, 0, 0);
;   od = __builtin_amdgcn_mfma_f32_32x32x16_bf16(pa2, PK(l2, h2), od, 0, 0, 0);
;   od = __builtin_amdgcn_mfma_f32_32x32x16_bf16(pa3, PK(l3, h3), od, 0, 0, 0);
;     ...
; }
; __device__ __forceinline__ void pv_d0(f32x16* o, int vb, bf16x8 pa0, bf16x8 pa1, bf16x8 pa2, bf16x8 pa3) {
;   pv_one<0>(o[0], vb, pa0, pa1, pa2, pa3); pv_one<1>(o[1], vb, pa0, pa1, pa2, pa3); pv_one<2>(o[2], vb, pa0, pa1, pa2, pa3); pv_one<3>(o[3], vb, pa0, pa1, pa2, pa3);
; template <bool HALF> __device__ __forceinline__ void dense_body(const bf16_t* __restrict__ Qb, const bf16_t* __restrict__ Kh, const bf16_t* __restrict__ Vh, ...
;     ...
;   pv_d0(o, vb0, pa0, pa1, pa2, pa3); partialSM(pB0, pB1, m_reg, mnB, alB);
;   __syncthreads(); RESC(alB);
	v_mfma_f32_32x32x16_bf16 v[48:63], v[100:103], v[116:119], v[48:63]
	ds_read_b64_tr_b16 v[116:117], v187 offset:0x400
	ds_read_b64_tr_b16 v[118:119], v187 offset:0xc00
	v_mfma_f32_32x32x16_bf16 v[48:63], v[104:107], v[120:123], v[48:63]
	ds_read_b64_tr_b16 v[120:121], v187 offset:0x1400
	ds_read_b64_tr_b16 v[122:123], v187 offset:0x1c00
	v_mfma_f32_32x32x16_bf16 v[48:63], v[108:111], v[124:127], v[48:63]
	ds_read_b64_tr_b16 v[124:125], v187 offset:0x2400
	ds_read_b64_tr_b16 v[126:127], v187 offset:0x2c00
	v_mfma_f32_32x32x16_bf16 v[48:63], v[112:115], v[128:131], v[48:63]
	ds_read_b64_tr_b16 v[128:129], v187 offset:0x3400
	ds_read_b64_tr_b16 v[130:131], v187 offset:0x3c00
	s_waitcnt lgkmcnt(0)
	v_mfma_f32_32x32x16_bf16 v[32:47], v[100:103], v[116:119], v[32:47]
	ds_read_b64_tr_b16 v[116:117], v187 offset:0x600
	ds_read_b64_tr_b16 v[118:119], v187 offset:0xe00
	v_mfma_f32_32x32x16_bf16 v[32:47], v[104:107], v[120:123], v[32:47]
	ds_read_b64_tr_b16 v[120:121], v187 offset:0x1600
	ds_read_b64_tr_b16 v[122:123], v187 offset:0x1e00
	v_mfma_f32_32x32x16_bf16 v[32:47], v[108:111], v[124:127], v[32:47]
	ds_read_b64_tr_b16 v[124:125], v187 offset:0x2600
	ds_read_b64_tr_b16 v[126:127], v187 offset:0x2e00
	v_mfma_f32_32x32x16_bf16 v[32:47], v[112:115], v[128:131], v[32:47]
	ds_read_b64_tr_b16 v[128:129], v187 offset:0x3600
	ds_read_b64_tr_b16 v[130:131], v187 offset:0x3e00
	s_waitcnt lgkmcnt(0)
	v_mfma_f32_32x32x16_bf16 v[16:31], v[100:103], v[116:119], v[16:31]
	v_max_f32_e32 v100, v81, v81
	v_max_f32_e32 v101, v80, v80
	v_max_f32_e32 v100, v101, v100
	v_max3_f32 v100, v100, v82, v83
	v_max3_f32 v100, v100, v84, v85
	v_max3_f32 v100, v100, v86, v87
	v_max3_f32 v100, v100, v88, v89
	v_max3_f32 v100, v100, v90, v91
	v_max3_f32 v100, v100, v92, v93
	v_mfma_f32_32x32x16_bf16 v[16:31], v[104:107], v[120:123], v[16:31]
	v_max3_f32 v100, v100, v94, v95
	v_max3_f32 v100, v100, v64, v65
	v_max3_f32 v100, v100, v66, v67
	v_max3_f32 v100, v100, v68, v69
	v_max3_f32 v100, v100, v70, v71
	v_max3_f32 v100, v100, v72, v73
	v_max3_f32 v100, v100, v74, v75
	v_max3_f32 v100, v100, v76, v77
	v_mfma_f32_32x32x16_bf16 v[16:31], v[108:111], v[124:127], v[16:31]
	v_max3_f32 v100, v100, v78, v79
	v_mov_b32_e32 v101, v100
	s_nop 1
	v_permlane32_swap_b32_e32 v100, v101
	v_max_f32_e32 v101, v101, v101
	v_max_f32_e32 v100, v100, v100
	v_max_f32_e32 v100, v100, v101
	v_sub_f32_e32 v101, v100, v150
	v_cmp_ge_f32_e32 vcc, s87, v101
	v_max_f32_e32 v101, v150, v150
	v_max_f32_e32 v101, v101, v100
	v_mfma_f32_32x32x16_bf16 v[16:31], v[112:115], v[128:131], v[16:31]
	v_sub_f32_e32 v100, v150, v101
	v_mul_f32_e32 v100, 0x3e0293ee, v100
	v_exp_f32_e32 v100, v100
	s_cmp_eq_u64 vcc, exec
	s_cselect_b64 s[42:43], -1, 0
	v_cndmask_b32_e64 v100, v100, 1.0, s[42:43]
	v_cmp_gt_f32_e32 vcc, 1.0, v100
	s_waitcnt vmcnt(0)
	s_barrier
	s_cbranch_vccz .LBB0_470
	s_and_saveexec_b64 s[6:7], s[40:41]
	ds_write_b32 v184, v100 offset:128
	s_or_b64 exec, exec, s[6:7]
	s_waitcnt lgkmcnt(0)
	v_add_u32_e32 v114, v183, v96
	ds_read_b128 v[102:105], v114 offset:224
	ds_read_b128 v[106:109], v114 offset:192
	ds_read_b128 v[110:113], v114 offset:160
	ds_read_b128 v[114:117], v114 offset:128
	s_waitcnt lgkmcnt(3)
	v_pk_mul_f32 v[12:13], v[12:13], v[102:103]
	s_waitcnt lgkmcnt(2)
	v_pk_mul_f32 v[8:9], v[8:9], v[106:107]
	s_waitcnt lgkmcnt(1)
	v_pk_mul_f32 v[4:5], v[4:5], v[110:111]
	v_pk_mul_f32 v[14:15], v[14:15], v[104:105]
	v_pk_mul_f32 v[10:11], v[10:11], v[108:109]
	v_pk_mul_f32 v[6:7], v[6:7], v[112:113]
	s_waitcnt lgkmcnt(0)
	v_pk_mul_f32 v[2:3], v[2:3], v[116:117]
	v_pk_mul_f32 v[0:1], v[0:1], v[114:115]
	v_pk_mul_f32 v[60:61], v[60:61], v[102:103]
	v_pk_mul_f32 v[56:57], v[56:57], v[106:107]
	v_pk_mul_f32 v[52:53], v[52:53], v[110:111]
	v_pk_mul_f32 v[62:63], v[62:63], v[104:105]
	v_pk_mul_f32 v[58:59], v[58:59], v[108:109]
	v_pk_mul_f32 v[54:55], v[54:55], v[112:113]
	v_pk_mul_f32 v[50:51], v[50:51], v[116:117]
	v_pk_mul_f32 v[48:49], v[48:49], v[114:115]
	v_pk_mul_f32 v[44:45], v[44:45], v[102:103]
	v_pk_mul_f32 v[40:41], v[40:41], v[106:107]
	v_pk_mul_f32 v[36:37], v[36:37], v[110:111]
	v_pk_mul_f32 v[46:47], v[46:47], v[104:105]
	v_pk_mul_f32 v[42:43], v[42:43], v[108:109]
	v_pk_mul_f32 v[38:39], v[38:39], v[112:113]
	v_pk_mul_f32 v[34:35], v[34:35], v[116:117]
	v_pk_mul_f32 v[32:33], v[32:33], v[114:115]
	v_pk_mul_f32 v[28:29], v[28:29], v[102:103]
	v_pk_mul_f32 v[24:25], v[24:25], v[106:107]
	v_pk_mul_f32 v[20:21], v[20:21], v[110:111]
	v_pk_mul_f32 v[30:31], v[30:31], v[104:105]
	v_pk_mul_f32 v[26:27], v[26:27], v[108:109]
	v_pk_mul_f32 v[22:23], v[22:23], v[112:113]
	v_pk_mul_f32 v[18:19], v[18:19], v[116:117]
	v_pk_mul_f32 v[16:17], v[16:17], v[114:115]
